# baseline (speedup 1.0000x reference)
.LBB1_27:
	s_waitcnt lgkmcnt(0)
	s_barrier
	s_lshl_b32 s10, s9, 14
	s_lshl_b32 s13, 1, s0
	s_and_b32 s0, s13, s4
	v_or_b32_e32 v10, s10, v89
	s_cmp_eq_u32 s0, 0
	v_add_u32_e32 v106, v10, v1
	v_add_u32_e32 v105, s10, v91
	s_cbranch_scc1 .LBB1_37
	ds_read_b128 v[58:61], v106
	ds_read_b128 v[62:65], v105
	v_lshrrev_b64 v[10:11], v98, v[102:103]
	v_bfe_i32 v13, v10, 1, 1
	v_bfe_i32 v31, v10, 2, 1
	s_waitcnt lgkmcnt(1)
	v_mfma_f32_16x16x32_f16 v[58:61], v[58:61], v[2:5], v[120:123]
	v_bfe_i32 v32, v10, 3, 1
	v_bfe_i32 v11, v10, 0, 1
	s_waitcnt lgkmcnt(0)
	v_mfma_f32_16x16x32_f16 v[58:61], v[62:65], v[6:9], v[58:61]
	s_nop 7
	v_bitop3_b32 v10, v59, s5, v13 bitop3:0xe4
	v_bitop3_b32 v31, v60, s5, v31 bitop3:0xe4
	v_bitop3_b32 v13, v61, s5, v32 bitop3:0xe4
	v_max_f32_e32 v32, v13, v13
	v_max_f32_e32 v33, v31, v31
	v_bitop3_b32 v11, v58, s5, v11 bitop3:0xe4
	v_max_f32_e32 v32, v33, v32
	v_max3_f32 v32, v11, v10, v32
	v_cmp_lt_f32_e32 vcc, s7, v32
	s_or_b64 s[0:1], s[14:15], vcc
	s_cbranch_scc0 .LBB1_35
	v_and_b32_e32 v58, 64, v0
	v_xor_b32_e32 v33, 16, v0
	v_add_u32_e32 v58, 64, v58
	v_cmp_lt_i32_e32 vcc, v33, v58
	s_mov_b64 s[22:23], 0
	s_nop 0
	v_cndmask_b32_e32 v33, v0, v33, vcc
	v_lshlrev_b32_e32 v33, 2, v33
	ds_bpermute_b32 v33, v33, v32
	v_max_f32_e32 v32, v32, v32
	s_waitcnt lgkmcnt(0)
	v_max_f32_e32 v33, v33, v33
	v_max_f32_e32 v32, v32, v33
	v_mov_b32_e32 v33, v32
	s_nop 1
	v_permlane32_swap_b32_e32 v32, v33
	v_max_f32_e32 v33, v33, v33
	v_max_f32_e32 v32, v32, v32
	v_max_f32_e32 v32, v32, v33
	v_cmp_nlg_f32_e32 vcc, s5, v32
	v_cmp_lg_f32_e64 s[0:1], s5, v32
	s_and_saveexec_b64 s[24:25], s[0:1]
	v_cmp_lt_f32_e64 s[0:1], s7, v32
	s_or_b64 s[0:1], s[14:15], s[0:1]
	s_and_b64 s[22:23], s[0:1], exec
	s_or_b64 exec, exec, s[24:25]
	v_exp_f32_e64 v33, -v32
	v_cndmask_b32_e64 v32, 0, v32, s[22:23]
	v_sub_f32_e32 v11, v11, v32
	v_sub_f32_e32 v10, v10, v32
	v_cndmask_b32_e64 v33, v33, 1.0, s[14:15]
	v_cndmask_b32_e64 v66, 1.0, v33, s[22:23]
	v_pk_mul_f32 v[48:49], v[48:49], v[66:67] op_sel_hi:[1,0]
	v_pk_mul_f32 v[46:47], v[46:47], v[66:67] op_sel_hi:[1,0]
	v_pk_mul_f32 v[44:45], v[66:67], v[44:45] op_sel_hi:[0,1]
	v_pk_mul_f32 v[42:43], v[66:67], v[42:43] op_sel_hi:[0,1]
	v_pk_mul_f32 v[40:41], v[66:67], v[40:41] op_sel_hi:[0,1]
	v_pk_mul_f32 v[38:39], v[66:67], v[38:39] op_sel_hi:[0,1]
	v_pk_mul_f32 v[36:37], v[66:67], v[36:37] op_sel_hi:[0,1]
	v_pk_mul_f32 v[34:35], v[66:67], v[34:35] op_sel_hi:[0,1]
	v_pk_mul_f32 v[52:53], v[52:53], v[66:67] op_sel_hi:[1,0]
	v_pk_mul_f32 v[50:51], v[50:51], v[66:67] op_sel_hi:[1,0]
	v_sub_f32_e32 v31, v31, v32
	v_sub_f32_e32 v13, v13, v32
	v_sub_f32_e32 v120, v120, v32
	v_sub_f32_e32 v121, v121, v32
	v_sub_f32_e32 v122, v122, v32
	v_sub_f32_e32 v123, v123, v32
	s_and_b64 s[0:1], s[14:15], vcc
	s_branch .LBB1_36

.LBB1_36:
	v_add_u32_e32 v107, s10, v87
	v_exp_f32_e32 v31, v31
	v_exp_f32_e32 v13, v13
	ds_read_b128 v[70:73], v107 offset:8192
	v_exp_f32_e32 v74, v11
	v_exp_f32_e32 v10, v10
	ds_read_b128 v[66:69], v107 offset:10240
	v_cvt_pkrtz_f16_f32 v11, v31, v13
	v_cvt_pkrtz_f16_f32 v10, v74, v10
	v_mov_b32_e32 v13, v12
	ds_read_b128 v[58:61], v107 offset:12288
	ds_read_b128 v[108:111], v107 offset:14336
	v_mfma_f32_16x16x32_f16 v[50:53], v[114:117], v[10:13], v[50:53]
	s_waitcnt lgkmcnt(3)
	v_mfma_f32_16x16x32_f16 v[46:49], v[70:73], v[10:13], v[46:49]
	s_waitcnt lgkmcnt(2)
	v_mfma_f32_16x16x32_f16 v[42:45], v[66:69], v[10:13], v[42:45]
	s_waitcnt lgkmcnt(1)
	v_mfma_f32_16x16x32_f16 v[38:41], v[58:61], v[10:13], v[38:41]
	s_waitcnt lgkmcnt(0)
	v_mfma_f32_16x16x32_f16 v[34:37], v[108:111], v[10:13], v[34:37]
	s_branch .Lat_tail

.Lat_tail:
	s_andn2_b64 vcc, exec, s[18:19]
	s_cbranch_vccnz .Lat_exit4
	s_xor_b32 s9, s9, 1
	s_lshl_b32 s10, s9, 14
	s_waitcnt vmcnt(0)
	v_or_b32_e32 v10, s10, v99
	v_mov_b64_e32 v[102:103], v[100:101]
	v_or_b32_e32 v11, s10, v90
	ds_write_b128 v10, v[22:25]
	ds_write_b128 v11, v[14:17] offset:8192
	ds_write_b128 v10, v[18:21] offset:4096
	ds_write_b128 v11, v[26:29] offset:12288
	s_mov_b64 s[14:15], s[0:1]
	s_mov_b32 s0, s16
	s_cmp_gt_i32 s11, 3
	s_cbranch_scc1 .LBB1_17
	s_branch .LBB1_20
.Lat_exit4:
	s_nop 7
	v_mov_b64_e32 v[58:59], v[34:35]
	v_mov_b64_e32 v[60:61], v[36:37]
	v_mov_b64_e32 v[62:63], v[38:39]
	v_mov_b64_e32 v[64:65], v[40:41]
	v_mov_b64_e32 v[66:67], v[42:43]
	v_mov_b64_e32 v[68:69], v[44:45]
	v_mov_b64_e32 v[70:71], v[46:47]
	v_mov_b64_e32 v[72:73], v[48:49]
	v_mov_b64_e32 v[74:75], v[50:51]
	v_mov_b64_e32 v[76:77], v[52:53]
	s_branch .LBB1_47
.LBB1_47:
	v_div_scale_f32 v0, s[0:1], v74, v74, 1.0
	v_rcp_f32_e32 v1, v0
	v_div_scale_f32 v2, vcc, 1.0, v74, 1.0
	s_lshl_b32 s0, s3, 7
	v_fma_f32 v3, -v0, v1, 1.0
	v_fmac_f32_e32 v1, v3, v1
	v_mul_f32_e32 v3, v2, v1
	v_fma_f32 v4, -v0, v3, v2
	v_fmac_f32_e32 v3, v4, v1
	v_fma_f32 v0, -v0, v3, v2
	v_div_fmas_f32 v0, v0, v1, v3
	s_and_b32 s0, s0, 0x800
	v_div_fixup_f32 v4, v0, v74, 1.0
	v_add_u32_e32 v0, s0, v86
	v_ashrrev_i32_e32 v1, 31, v0
	v_lshlrev_b64 v[0:1], 11, v[0:1]
	s_lshl_b32 s0, s2, 7
	v_lshl_add_u64 v[0:1], s[20:21], 0, v[0:1]
	s_and_b32 s0, s0, 0x780
	s_mov_b32 s1, 0
	v_lshl_add_u64 v[0:1], v[0:1], 0, s[0:1]
	v_lshlrev_b32_e32 v2, 1, v88
	v_mov_b32_e32 v3, 0
	v_lshl_add_u64 v[6:7], v[0:1], 0, v[2:3]
	v_mov_b32_e32 v0, v71
	v_mov_b32_e32 v1, v72
	v_pk_mul_f32 v[0:1], v[4:5], v[0:1] op_sel_hi:[0,1]
	v_fma_mixlo_f16 v2, v4, v70, 0
	v_cvt_pk_f16_f32 v1, v0, v1
	v_pack_b32_f16 v0, v2, v1
	v_mov_b32_e32 v2, v67
	v_mov_b32_e32 v3, v68
	v_pk_mul_f32 v[2:3], v[4:5], v[2:3] op_sel_hi:[0,1]
	v_cvt_pk_f16_f32 v5, v2, v3
	v_pk_mov_b32 v[2:3], v[72:73], v[66:67] op_sel:[1,0]
	s_nop 0
	v_pk_mul_f32 v[2:3], v[4:5], v[2:3] op_sel_hi:[0,1]
	v_cvt_pk_f16_f32 v2, v2, v3
	v_lshrrev_b32_e32 v3, 16, v5
	v_alignbit_b32 v1, v2, v1, 16
	v_alignbit_b32 v2, v5, v2, 16
	v_fma_mixhi_f16 v3, v4, v69, 0
	global_store_dwordx4 v[6:7], v[0:3], off sc1
	s_nop 1
	v_mov_b32_e32 v0, v63
	v_mov_b32_e32 v1, v64
	v_pk_mul_f32 v[0:1], v[4:5], v[0:1] op_sel_hi:[0,1]
	v_fma_mixlo_f16 v2, v4, v62, 0
	v_cvt_pk_f16_f32 v1, v0, v1
	v_pack_b32_f16 v0, v2, v1
	v_mov_b32_e32 v2, v59
	v_mov_b32_e32 v3, v60
	v_pk_mul_f32 v[2:3], v[4:5], v[2:3] op_sel_hi:[0,1]
	v_cvt_pk_f16_f32 v5, v2, v3
	v_pk_mov_b32 v[2:3], v[64:65], v[58:59] op_sel:[1,0]
	s_nop 0
	v_pk_mul_f32 v[2:3], v[4:5], v[2:3] op_sel_hi:[0,1]
	v_cvt_pk_f16_f32 v2, v2, v3
	v_lshrrev_b32_e32 v3, 16, v5
	v_alignbit_b32 v1, v2, v1, 16
	v_alignbit_b32 v2, v5, v2, 16
	v_fma_mixhi_f16 v3, v4, v61, 0
	global_store_dwordx4 v[6:7], v[0:3], off offset:64 sc1
